# 64 helper WGs + 192 workers in layer-0 MoE phases (6 tile rounds), 24576 layer-1 conversion items deferred from the prologue to the helpers
# speedup vs baseline: 1.0168x; 1.0035x over previous
;     ...
;         while (it < NIT) {
;             const int itB = it + NGW;
;             if (itB < NIT) { dB = decode(NIT - 1 - itB); tr_load(dB, vB); }
;             tr_finish(dA, vA, scr, lane);
;             if (itB >= NIT) break;
;             const int itA = itB + NGW;
;             if (itA < NIT) { dA = decode(NIT - 1 - itA); tr_load(dA, vA); }
;             tr_finish(dB, vB, scr, lane);
;             it = itA;
.LBB0_72:
	s_cmp_gt_i32 s42, 0xfcff
	s_cbranch_scc1 .LBB0_70
	s_add_i32 s44, s42, s48
	s_cmpk_lt_i32 s44, 0x6800
	s_cbranch_scc0 .Lps_1
	s_add_i32 s44, s44, 0x6000

; #define LAS __attribute__((address_space(3)))
; #define GAS __attribute__((address_space(1)))
; #define LDS_WAIT() asm volatile("s_waitcnt lgkmcnt(0)" ::: "memory")
; __device__ __forceinline__ unsigned pk_fp8x4(float a, float b, float c, float d) { int p = __builtin_amdgcn_cvt_pk_fp8_f32(sat8(a), sat8(b), 0, false); p = __builtin_amdgcn_cvt_pk_fp8_f32(sat8(c), sat8(d), p, true); return (unsigned)p; }
; __device__ __forceinline__ void tr_finish(const TrDesc& d, f32x4 (&v)[16], LAS float* scr, int lane) {
;     ...
;     { LAS float* rp = scr + kk * 65 + d0;
; #pragma unroll
;         for (int i = 0; i < 16; ++i) { rp[4 * i * 65] = v[i][0]; rp[4 * i * 65 + ds] = v[i][1]; rp[4 * i * 65 + 2 * ds] = v[i][2]; rp[4 * i * 65 + 3 * ds] = v[i][3]; } }
;     LDS_WAIT(); asm volatile("" ::: "memory");
;     if (d.f8) {
;         const int c = lane & 3, nl = lane >> 2; const LAS float* sp = scr + (16 * c) * 65 + nl; unsigned char* dp = d.dst + (size_t)nl * d.K + 16 * c;
; #pragma unroll
;         for (int j = 0; j < 4; ++j) { u32x4 o;
;             o.x = pk_fp8x4(sp[0 * 65 + 16 * j] * 32.0f, sp[1 * 65 + 16 * j] * 32.0f, sp[2 * 65 + 16 * j] * 32.0f, sp[3 * 65 + 16 * j] * 32.0f);
;             o.y = pk_fp8x4(sp[4 * 65 + 16 * j] * 32.0f, sp[5 * 65 + 16 * j] * 32.0f, sp[6 * 65 + 16 * j] * 32.0f, sp[7 * 65 + 16 * j] * 32.0f);
;             o.z = pk_fp8x4(sp[8 * 65 + 16 * j] * 32.0f, sp[9 * 65 + 16 * j] * 32.0f, sp[10 * 65 + 16 * j] * 32.0f, sp[11 * 65 + 16 * j] * 32.0f);
;             o.w = pk_fp8x4(sp[12 * 65 + 16 * j] * 32.0f, sp[13 * 65 + 16 * j] * 32.0f, sp[14 * 65 + 16 * j] * 32.0f, sp[15 * 65 + 16 * j] * 32.0f);
;             *(GAS u32x4*)(dp + (size_t)(16 * j) * d.K) = o; }
.LBB0_108:
	s_or_b64 exec, exec, s[22:23]
	s_cmp_eq_u32 s43, 0
	s_cselect_b64 vcc, -1, 0
	s_cmp_lg_u32 s43, 0
	s_cselect_b64 s[22:23], -1, 0
	v_cndmask_b32_e64 v2, 0, 1, s[22:23]
	s_and_b64 s[22:23], s[22:23], exec
	v_cndmask_b32_e32 v0, v140, v136, vcc
	s_cselect_b32 s0, 2, 1
	v_lshl_add_u32 v0, v0, 2, v141
	s_lshl_b32 s3, s0, 2
	v_add_u32_e32 v3, s3, v0
	v_lshlrev_b32_e64 v2, v2, 3
	s_waitcnt vmcnt(15)
	ds_write_b32 v3, v5
	v_lshl_add_u32 v3, s0, 3, v0
	v_lshl_add_u32 v2, v2, 2, v0
	v_subrev_u32_e32 v146, s3, v3
	ds_write_b32 v0, v4
	ds_write_b32 v3, v6
	ds_write_b32 v2, v7
	s_waitcnt vmcnt(14)
	ds_write_b32 v0, v8 offset:1040
	ds_write_b32 v146, v9 offset:1040
	ds_write_b32 v3, v10 offset:1040
	ds_write_b32 v2, v11 offset:1040
	s_waitcnt vmcnt(13)
	ds_write_b32 v0, v12 offset:2080
	ds_write_b32 v146, v13 offset:2080
	ds_write_b32 v3, v14 offset:2080
	ds_write_b32 v2, v15 offset:2080
	s_waitcnt vmcnt(12)
	ds_write_b32 v0, v16 offset:3120
	ds_write_b32 v146, v17 offset:3120
	ds_write_b32 v3, v18 offset:3120
	ds_write_b32 v2, v19 offset:3120
	s_waitcnt vmcnt(11)
	ds_write_b32 v0, v20 offset:4160
	ds_write_b32 v146, v21 offset:4160
	ds_write_b32 v3, v22 offset:4160
	ds_write_b32 v2, v23 offset:4160
	s_waitcnt vmcnt(10)
	ds_write_b32 v0, v24 offset:5200
	ds_write_b32 v146, v25 offset:5200
	ds_write_b32 v3, v26 offset:5200
	ds_write_b32 v2, v27 offset:5200
	s_waitcnt vmcnt(9)
	ds_write_b32 v0, v28 offset:6240
	ds_write_b32 v146, v29 offset:6240
	ds_write_b32 v3, v30 offset:6240
	ds_write_b32 v2, v31 offset:6240
	s_waitcnt vmcnt(8)
	ds_write_b32 v0, v32 offset:7280
	ds_write_b32 v146, v33 offset:7280
	ds_write_b32 v3, v34 offset:7280
	ds_write_b32 v2, v35 offset:7280
	s_waitcnt vmcnt(7)
	ds_write_b32 v0, v36 offset:8320
	ds_write_b32 v146, v37 offset:8320
	ds_write_b32 v3, v38 offset:8320
	ds_write_b32 v2, v39 offset:8320
	s_waitcnt vmcnt(6)
	ds_write_b32 v0, v40 offset:9360
	ds_write_b32 v146, v41 offset:9360
	ds_write_b32 v3, v42 offset:9360
	ds_write_b32 v2, v43 offset:9360
	s_waitcnt vmcnt(5)
	ds_write_b32 v0, v44 offset:10400
	ds_write_b32 v146, v45 offset:10400
	ds_write_b32 v3, v46 offset:10400
	ds_write_b32 v2, v47 offset:10400
	s_waitcnt vmcnt(4)
	ds_write_b32 v0, v48 offset:11440
	ds_write_b32 v146, v49 offset:11440
	ds_write_b32 v3, v50 offset:11440
	ds_write_b32 v2, v51 offset:11440
	s_waitcnt vmcnt(3)
	ds_write_b32 v0, v52 offset:12480
	ds_write_b32 v146, v53 offset:12480
	ds_write_b32 v3, v54 offset:12480
	ds_write_b32 v2, v55 offset:12480
	s_waitcnt vmcnt(2)
	ds_write_b32 v0, v56 offset:13520
	ds_write_b32 v146, v57 offset:13520
	ds_write_b32 v3, v58 offset:13520
	ds_write_b32 v2, v59 offset:13520
	s_waitcnt vmcnt(1)
	ds_write_b32 v0, v60 offset:14560
	ds_write_b32 v146, v61 offset:14560
	ds_write_b32 v3, v62 offset:14560
	ds_write_b32 v2, v63 offset:14560
	s_waitcnt vmcnt(0)
	ds_write_b32 v0, v64 offset:15600
	ds_write_b32 v146, v65 offset:15600
	ds_write_b32 v3, v66 offset:15600
	ds_write_b32 v2, v67 offset:15600
	s_waitcnt lgkmcnt(0)
	ds_read2_b32 v[2:3], v142 offset1:16
	ds_read2_b32 v[148:149], v142 offset0:65 offset1:81
	ds_read2_b32 v[154:155], v142 offset0:130 offset1:146
	ds_read2_b32 v[156:157], v142 offset0:195 offset1:211
	v_mov_b32_e32 v150, 0
	s_waitcnt lgkmcnt(3)
	v_mul_f32_e32 v0, 0x42000000, v2
	s_waitcnt lgkmcnt(2)
	v_mul_f32_e32 v2, 0x42000000, v148
	v_med3_f32 v0, v0, s41, v143
	s_waitcnt lgkmcnt(0)
	v_mul_f32_e32 v147, 0x42000000, v156
	v_med3_f32 v2, v2, s41, v143
	v_cvt_pk_fp8_f32 v150, v0, v2
	v_med3_f32 v2, v147, s41, v143
	v_add_u32_e32 v147, 0x400, v142
	ds_read2_b32 v[160:161], v147 offset0:4 offset1:20
	ds_read2_b32 v[162:163], v147 offset0:69 offset1:85
	ds_read2_b32 v[164:165], v147 offset0:134 offset1:150
	ds_read2_b32 v[166:167], v147 offset0:199 offset1:215
	v_mul_f32_e32 v146, 0x42000000, v154
	v_med3_f32 v0, v146, s41, v143
	v_cvt_pk_fp8_f32 v150, v0, v2 op_sel:[0,0,1]
	s_waitcnt lgkmcnt(3)
	v_mul_f32_e32 v0, 0x42000000, v160
	s_waitcnt lgkmcnt(2)
	v_mul_f32_e32 v2, 0x42000000, v162
	s_waitcnt lgkmcnt(0)
	v_mul_f32_e32 v148, 0x42000000, v166
	v_med3_f32 v0, v0, s41, v143
	v_med3_f32 v2, v2, s41, v143
	v_mov_b32_e32 v151, 0
	v_cvt_pk_fp8_f32 v151, v0, v2
	v_med3_f32 v2, v148, s41, v143
	v_add_u32_e32 v148, 0x800, v142
	ds_read2_b32 v[168:169], v148 offset0:8 offset1:24
	ds_read2_b32 v[170:171], v148 offset0:73 offset1:89
	ds_read2_b32 v[172:173], v148 offset0:138 offset1:154
	ds_read2_b32 v[174:175], v148 offset0:203 offset1:219
	v_mul_f32_e32 v146, 0x42000000, v164
	v_med3_f32 v0, v146, s41, v143
	v_cvt_pk_fp8_f32 v151, v0, v2 op_sel:[0,0,1]
	s_waitcnt lgkmcnt(3)
	v_mul_f32_e32 v0, 0x42000000, v168
	s_waitcnt lgkmcnt(2)
	v_mul_f32_e32 v2, 0x42000000, v170
	s_waitcnt lgkmcnt(1)
	v_mul_f32_e32 v146, 0x42000000, v172
	v_med3_f32 v0, v0, s41, v143
	v_med3_f32 v2, v2, s41, v143
	v_mov_b32_e32 v152, 0
	v_cvt_pk_fp8_f32 v152, v0, v2
	v_med3_f32 v0, v146, s41, v143
	v_add_u32_e32 v146, 0xc00, v142
	ds_read2_b32 v[176:177], v146 offset0:12 offset1:28
	ds_read2_b32 v[178:179], v146 offset0:77 offset1:93
	ds_read2_b32 v[180:181], v146 offset0:142 offset1:158
	s_waitcnt lgkmcnt(3)
	v_mul_f32_e32 v153, 0x42000000, v174
	v_med3_f32 v2, v153, s41, v143
	ds_read2_b32 v[182:183], v146 offset0:207 offset1:223
	v_cvt_pk_fp8_f32 v152, v0, v2 op_sel:[0,0,1]
	s_waitcnt lgkmcnt(3)
	v_mul_f32_e32 v0, 0x42000000, v176
	s_waitcnt lgkmcnt(2)
	v_mul_f32_e32 v2, 0x42000000, v178
	v_med3_f32 v0, v0, s41, v143
	v_med3_f32 v2, v2, s41, v143
	v_mov_b32_e32 v153, 0
	v_cvt_pk_fp8_f32 v153, v0, v2
	s_waitcnt lgkmcnt(1)
	v_mul_f32_e32 v154, 0x42000000, v180
	s_waitcnt lgkmcnt(0)
; #define GAS __attribute__((address_space(1)))
; __device__ __forceinline__ unsigned pk_fp8x4(float a, float b, float c, float d) { int p = __builtin_amdgcn_cvt_pk_fp8_f32(sat8(a), sat8(b), 0, false); p = __builtin_amdgcn_cvt_pk_fp8_f32(sat8(c), sat8(d), p, true); return (unsigned)p; }
; __device__ __forceinline__ void tr_finish(const TrDesc& d, f32x4 (&v)[16], LAS float* scr, int lane) {
;     ...
;         for (int j = 0; j < 4; ++j) { u32x4 o;
;             o.x = pk_fp8x4(sp[0 * 65 + 16 * j] * 32.0f, sp[1 * 65 + 16 * j] * 32.0f, sp[2 * 65 + 16 * j] * 32.0f, sp[3 * 65 + 16 * j] * 32.0f);
;             o.y = pk_fp8x4(sp[4 * 65 + 16 * j] * 32.0f, sp[5 * 65 + 16 * j] * 32.0f, sp[6 * 65 + 16 * j] * 32.0f, sp[7 * 65 + 16 * j] * 32.0f);
;             o.z = pk_fp8x4(sp[8 * 65 + 16 * j] * 32.0f, sp[9 * 65 + 16 * j] * 32.0f, sp[10 * 65 + 16 * j] * 32.0f, sp[11 * 65 + 16 * j] * 32.0f);
;             o.w = pk_fp8x4(sp[12 * 65 + 16 * j] * 32.0f, sp[13 * 65 + 16 * j] * 32.0f, sp[14 * 65 + 16 * j] * 32.0f, sp[15 * 65 + 16 * j] * 32.0f);
;             *(GAS u32x4*)(dp + (size_t)(16 * j) * d.K) = o; }
;     ...
;             if (itB >= NIT) break;
;             const int itA = itB + NGW;
;             if (itA < NIT) { dA = decode(NIT - 1 - itA); tr_load(dA, vA); }
	v_mul_f32_e32 v0, 0x42000000, v182
	v_med3_f32 v2, v154, s41, v143
	v_med3_f32 v0, v0, s41, v143
	v_cvt_pk_fp8_f32 v153, v2, v0 op_sel:[0,0,1]
	v_mov_b64_e32 v[158:159], s[16:17]
	v_mad_i64_i32 v[158:159], s[22:23], s2, v132, v[158:159]
	v_lshl_add_u64 v[158:159], v[158:159], 0, v[134:135]
	v_mul_f32_e32 v0, 0x42000000, v3
	v_mul_f32_e32 v2, 0x42000000, v149
	global_store_dwordx4 v[158:159], v[150:153], off
	v_med3_f32 v0, v0, s41, v143
	v_med3_f32 v2, v2, s41, v143
	v_mov_b32_e32 v150, 0
	v_cvt_pk_fp8_f32 v150, v0, v2
	v_mul_f32_e32 v3, 0x42000000, v155
	v_mul_f32_e32 v0, 0x42000000, v157
	v_med3_f32 v2, v3, s41, v143
	v_med3_f32 v0, v0, s41, v143
	v_cvt_pk_fp8_f32 v150, v2, v0 op_sel:[0,0,1]
	v_mul_f32_e32 v0, 0x42000000, v161
	v_mul_f32_e32 v2, 0x42000000, v163
	v_med3_f32 v0, v0, s41, v143
	v_med3_f32 v2, v2, s41, v143
	v_mov_b32_e32 v151, 0
	v_cvt_pk_fp8_f32 v151, v0, v2
	v_mul_f32_e32 v3, 0x42000000, v165
	v_mul_f32_e32 v0, 0x42000000, v167
	v_med3_f32 v2, v3, s41, v143
	v_med3_f32 v0, v0, s41, v143
	v_cvt_pk_fp8_f32 v151, v2, v0 op_sel:[0,0,1]
	v_mul_f32_e32 v0, 0x42000000, v169
	v_mul_f32_e32 v2, 0x42000000, v171
	v_med3_f32 v0, v0, s41, v143
	v_med3_f32 v2, v2, s41, v143
	v_mov_b32_e32 v152, 0
	v_cvt_pk_fp8_f32 v152, v0, v2
	v_mul_f32_e32 v3, 0x42000000, v173
	v_mul_f32_e32 v0, 0x42000000, v175
	v_med3_f32 v2, v3, s41, v143
	v_med3_f32 v0, v0, s41, v143
	v_cvt_pk_fp8_f32 v152, v2, v0 op_sel:[0,0,1]
	v_mul_f32_e32 v0, 0x42000000, v177
	v_mul_f32_e32 v2, 0x42000000, v179
	v_med3_f32 v0, v0, s41, v143
	v_med3_f32 v2, v2, s41, v143
	v_mov_b32_e32 v153, 0
	v_cvt_pk_fp8_f32 v153, v0, v2
	s_ashr_i32 s3, s2, 31
	v_mul_f32_e32 v3, 0x42000000, v181
	v_mul_f32_e32 v0, 0x42000000, v183
	v_med3_f32 v2, v3, s41, v143
	v_med3_f32 v0, v0, s41, v143
	s_lshl_b64 s[22:23], s[2:3], 4
	v_cvt_pk_fp8_f32 v153, v2, v0 op_sel:[0,0,1]
	v_lshl_add_u64 v[2:3], v[158:159], 0, s[22:23]
	ds_read2_b32 v[154:155], v142 offset0:32 offset1:48
	ds_read2_b32 v[156:157], v142 offset0:97 offset1:113
	ds_read2_b32 v[158:159], v142 offset0:162 offset1:178
	ds_read2_b32 v[160:161], v142 offset0:227 offset1:243
	s_andn2_b64 vcc, exec, s[20:21]
	s_waitcnt lgkmcnt(3)
	v_mul_f32_e32 v0, 0x42000000, v154
	s_waitcnt lgkmcnt(2)
	v_mul_f32_e32 v149, 0x42000000, v156
	global_store_dwordx4 v[2:3], v[150:153], off
	v_med3_f32 v0, v0, s41, v143
	v_med3_f32 v149, v149, s41, v143
	v_mov_b32_e32 v150, 0
	v_cvt_pk_fp8_f32 v150, v0, v149
	ds_read2_b32 v[162:163], v147 offset0:36 offset1:52
	ds_read2_b32 v[164:165], v147 offset0:101 offset1:117
	ds_read2_b32 v[166:167], v147 offset0:166 offset1:182
	ds_read2_b32 v[168:169], v147 offset0:231 offset1:247
	s_waitcnt lgkmcnt(5)
	v_mul_f32_e32 v151, 0x42000000, v158
	s_waitcnt lgkmcnt(4)
	v_mul_f32_e32 v152, 0x42000000, v160
	v_med3_f32 v0, v151, s41, v143
	v_med3_f32 v149, v152, s41, v143
	v_cvt_pk_fp8_f32 v150, v0, v149 op_sel:[0,0,1]
	s_waitcnt lgkmcnt(3)
	v_mul_f32_e32 v0, 0x42000000, v162
	s_waitcnt lgkmcnt(2)
	v_mul_f32_e32 v149, 0x42000000, v164
	v_med3_f32 v0, v0, s41, v143
	v_med3_f32 v149, v149, s41, v143
	v_mov_b32_e32 v151, 0
	v_cvt_pk_fp8_f32 v151, v0, v149
	ds_read2_b32 v[170:171], v148 offset0:40 offset1:56
	ds_read2_b32 v[172:173], v148 offset0:105 offset1:121
	ds_read2_b32 v[174:175], v148 offset0:170 offset1:186
	ds_read2_b32 v[176:177], v148 offset0:235 offset1:251
	s_waitcnt lgkmcnt(5)
	v_mul_f32_e32 v152, 0x42000000, v166
	s_waitcnt lgkmcnt(4)
	v_mul_f32_e32 v153, 0x42000000, v168
	v_med3_f32 v0, v152, s41, v143
	v_med3_f32 v149, v153, s41, v143
	v_cvt_pk_fp8_f32 v151, v0, v149 op_sel:[0,0,1]
	s_waitcnt lgkmcnt(3)
	v_mul_f32_e32 v0, 0x42000000, v170
	s_waitcnt lgkmcnt(2)
	v_mul_f32_e32 v149, 0x42000000, v172
	v_med3_f32 v0, v0, s41, v143
	v_med3_f32 v149, v149, s41, v143
	v_mov_b32_e32 v152, 0
	v_cvt_pk_fp8_f32 v152, v0, v149
	ds_read2_b32 v[178:179], v146 offset0:44 offset1:60
	ds_read2_b32 v[180:181], v146 offset0:109 offset1:125
	ds_read2_b32 v[182:183], v146 offset0:174 offset1:190
	s_waitcnt lgkmcnt(4)
	v_mul_f32_e32 v153, 0x42000000, v174
	s_waitcnt lgkmcnt(3)
	v_mul_f32_e32 v154, 0x42000000, v176
	v_med3_f32 v0, v153, s41, v143
	v_med3_f32 v149, v154, s41, v143
	ds_read2_b32 v[184:185], v146 offset0:239 offset1:255
	v_cvt_pk_fp8_f32 v152, v0, v149 op_sel:[0,0,1]
	s_waitcnt lgkmcnt(3)
	v_mul_f32_e32 v0, 0x42000000, v178
	s_waitcnt lgkmcnt(2)
	v_mul_f32_e32 v149, 0x42000000, v180
	v_med3_f32 v0, v0, s41, v143
	v_med3_f32 v149, v149, s41, v143
	v_mov_b32_e32 v153, 0
	v_cvt_pk_fp8_f32 v153, v0, v149
	s_waitcnt lgkmcnt(1)
	v_mul_f32_e32 v154, 0x42000000, v182
	s_waitcnt lgkmcnt(0)
	v_mul_f32_e32 v0, 0x42000000, v184
	v_med3_f32 v149, v154, s41, v143
	v_med3_f32 v0, v0, s41, v143
	v_cvt_pk_fp8_f32 v153, v149, v0 op_sel:[0,0,1]
	v_mul_f32_e32 v0, 0x42000000, v155
	v_mul_f32_e32 v149, 0x42000000, v157
	v_med3_f32 v0, v0, s41, v143
	v_med3_f32 v149, v149, s41, v143
	v_mov_b32_e32 v154, 0
	v_cvt_pk_fp8_f32 v154, v0, v149
	v_mul_f32_e32 v155, 0x42000000, v159
	v_mul_f32_e32 v0, 0x42000000, v161
	v_med3_f32 v149, v155, s41, v143
	v_med3_f32 v0, v0, s41, v143
	v_cvt_pk_fp8_f32 v154, v149, v0 op_sel:[0,0,1]
	v_mul_f32_e32 v0, 0x42000000, v163
	v_mul_f32_e32 v149, 0x42000000, v165
	v_med3_f32 v0, v0, s41, v143
	v_med3_f32 v149, v149, s41, v143
	v_mov_b32_e32 v155, 0
	v_cvt_pk_fp8_f32 v155, v0, v149
	v_mul_f32_e32 v156, 0x42000000, v167
	v_mul_f32_e32 v0, 0x42000000, v169
	v_med3_f32 v149, v156, s41, v143
	v_med3_f32 v0, v0, s41, v143
	v_cvt_pk_fp8_f32 v155, v149, v0 op_sel:[0,0,1]
	v_mul_f32_e32 v0, 0x42000000, v171
	v_mul_f32_e32 v149, 0x42000000, v173
	v_med3_f32 v0, v0, s41, v143
	v_med3_f32 v149, v149, s41, v143
	v_mov_b32_e32 v156, 0
	v_cvt_pk_fp8_f32 v156, v0, v149
	v_mul_f32_e32 v157, 0x42000000, v175
	v_mul_f32_e32 v0, 0x42000000, v177
	v_med3_f32 v149, v157, s41, v143
	v_med3_f32 v0, v0, s41, v143
	v_cvt_pk_fp8_f32 v156, v149, v0 op_sel:[0,0,1]
	v_mul_f32_e32 v0, 0x42000000, v179
	v_mul_f32_e32 v149, 0x42000000, v181
	v_med3_f32 v0, v0, s41, v143
	v_med3_f32 v149, v149, s41, v143
	v_mov_b32_e32 v157, 0
	v_cvt_pk_fp8_f32 v157, v0, v149
	v_mul_f32_e32 v158, 0x42000000, v183
	v_mul_f32_e32 v0, 0x42000000, v185
	v_med3_f32 v149, v158, s41, v143
	v_med3_f32 v0, v0, s41, v143
	v_cvt_pk_fp8_f32 v157, v149, v0 op_sel:[0,0,1]
	v_lshl_add_u64 v[2:3], v[2:3], 0, s[22:23]
	global_store_dwordx4 v[2:3], v[150:153], off
	v_lshl_add_u64 v[2:3], v[2:3], 0, s[22:23]
	global_store_dwordx4 v[2:3], v[154:157], off
	s_waitcnt lgkmcnt(0)
	s_cbranch_vccnz .LBB0_71
	s_add_i32 s42, s44, s48
	s_cmpk_lt_i32 s42, 0x6800
	s_cbranch_scc0 .Lps_2
	s_add_i32 s42, s42, 0x6000

; #define LAS __attribute__((address_space(3)))
; #define FRESH_TID() do { ap = fresh_args(); ws = ap->ws; unsigned m1_ = ~0u; asm volatile("" : "+s"(m1_)); lane = (int)__builtin_amdgcn_mbcnt_hi(m1_, __builtin_amdgcn_mbcnt_lo(m1_, 0u)); asm volatile("" : "+v"(lane)); wave = wave0; tid = wave0 * 64 + lane; } while (0)
; __device__ __forceinline__ void moe_table_build(LAS unsigned char* lds, const unsigned* cnt, int tid) {
;     if (tid < NE) { const int n = (int)__hip_atomic_load(cnt + 64 * tid, RLX_AGENT); ((LAS int*)(lds + MOE_TAB_OFF))[16 + tid] = n; }
; template <unsigned MASK, bool ONE>
; __global__ void __launch_bounds__(NTHREADS, 2) fwd_kernel(Args a_unused) {
;     ...
;         if (IN(P + 8, 9)) { FRESH_TID();
;             pg8::moe_table_build(lds, cntl, tid);
.LBB0_925:
	s_or_b64 exec, exec, s[0:1]
	v_readlane_b32 s101, v255, 17
	s_movk_i32 s100, 0x100
	s_cmp_eq_u32 s101, 0
	s_cselect_b32 s100, 0xc0, s100
	s_cselect_b32 s101, 64, 0
	v_readlane_b32 s0, v253, 0
	v_readlane_b32 s1, v253, 1
	s_waitcnt lgkmcnt(0)
	s_barrier
	s_load_dwordx2 s[6:7], s[0:1], 0xa0
	s_mov_b32 s0, s38
	s_nop 0
	v_mbcnt_lo_u32_b32 v0, s0, 0
	v_mbcnt_hi_u32_b32 v0, s0, v0
	s_nop 0
	v_add_u32_e32 v1, s78, v0
	v_cmp_gt_i32_e32 vcc, 16, v1
	s_and_saveexec_b64 s[0:1], vcc
	s_cbranch_execz .LBB0_927
	s_lshl_b64 s[2:3], s[96:97], 2
	s_waitcnt lgkmcnt(0)
	s_add_u32 s2, s6, s2
	v_lshlrev_b32_e32 v2, 6, v1
	s_addc_u32 s3, s7, s3
	v_ashrrev_i32_e32 v3, 31, v2
	v_lshl_add_u64 v[2:3], v[2:3], 2, s[2:3]
	v_add_co_u32_e32 v2, vcc, 0x10000, v2
	v_readlane_b32 s2, v255, 23
	s_nop 0
	v_addc_co_u32_e32 v3, vcc, 0, v3, vcc
	global_load_dword v2, v[2:3], off sc1
	v_lshl_add_u32 v3, v1, 2, s2
	s_waitcnt vmcnt(0)
	ds_write_b32 v3, v2 offset:64

; #define LAS __attribute__((address_space(3)))
; __device__ __forceinline__ void moe_table_build(LAS unsigned char* lds, const unsigned* cnt, int tid) {
;     ...
;     __syncthreads();
;     if (tid == 0) { int acc = 0; for (int e = 0; e < NE; ++e) { acc += (((LAS int*)(lds + MOE_TAB_OFF))[16 + e] + 255) >> 8; ((LAS int*)(lds + MOE_TAB_OFF))[e] = acc; } }
;     __syncthreads();
; }
;     __device__ __forceinline__ void init(LAS unsigned char* lds_, int nN_, int G_, int c_) {
;         lds = lds_; NT = __builtin_amdgcn_readfirstlane(((LAS int*)(lds + MOE_TAB_OFF))[15]); nN = nN_; G = G_; c = c_; }
.LBB0_929:
	s_or_b64 exec, exec, s[0:1]
	v_readlane_b32 s0, v254, 58
	s_waitcnt lgkmcnt(0)
	s_barrier
	v_mov_b32_e32 v2, s0
	ds_read_b32 v2, v2
	v_readlane_b32 s1, v253, 4
	v_readfirstlane_b32 s14, v1
	s_waitcnt lgkmcnt(0)
	v_readfirstlane_b32 s22, v2
	s_lshl_b32 s0, s22, 3
	s_cmp_eq_u32 s101, 0
	s_cbranch_scc1 .Lno_help9
	s_cmpk_lt_i32 s1, 0xc0
	s_cbranch_scc1 .Lno_help9
	s_movk_i32 s100, 0x800
	s_movk_i32 s101, 0x4600
	s_mov_b32 s0, 0
	v_writelane_b32 v251, s0, 30
	s_branch .Lhp_entry

; #define LAS __attribute__((address_space(3)))
;     ...
;         LAS float* scr = (LAS float*)(lds + wave * 16640);
;         const int gw = vcu * NWAVES + wave, NGW = G * NWAVES;
;         constexpr int C_IN = 32 * 188, C_OA = 8 * 32, C_OB = 16 * 32, C_O = 32 * 32, C_GU = 16 * 32 * 32, C_DN = 16 * 16 * 32, C_L = C_IN + C_OA + C_OB + C_O + C_GU + C_DN, NIT = DEPTH * C_L;
;         const int q4 = lane & 15, kk = lane >> 4;
;     ...
;         int it = gw; TrDesc dA, dB; f32x4 vA[16], vB[16];
;         if (it < NIT) { dA = decode(NIT - 1 - it); tr_load(dA, vA); }
.Lhp_entry:
	v_writelane_b32 v251, s16, 0
	v_writelane_b32 v251, s17, 1
	v_writelane_b32 v251, s18, 2
	v_writelane_b32 v251, s19, 3
	v_writelane_b32 v251, s20, 4
	v_writelane_b32 v251, s21, 5
	v_writelane_b32 v251, s23, 6
	v_writelane_b32 v251, s25, 7
	v_writelane_b32 v251, s26, 8
	v_writelane_b32 v251, s33, 9
	v_writelane_b32 v251, s38, 10
	v_writelane_b32 v251, s39, 11
	v_writelane_b32 v251, s41, 12
	v_writelane_b32 v251, s42, 13
	v_writelane_b32 v251, s45, 14
	v_writelane_b32 v251, s48, 15
	v_writelane_b32 v251, s49, 16
	v_writelane_b32 v251, s50, 17
	v_writelane_b32 v251, s51, 18
	v_writelane_b32 v251, s74, 19
	v_writelane_b32 v251, s76, 20
	v_mov_b32_e32 v193, v3
	v_mov_b32_e32 v194, v33
	v_mov_b32_e32 v195, v59
	v_mov_b32_e32 v196, v63
	v_mov_b32_e32 v197, v110
	v_mov_b32_e32 v198, v111
	v_mov_b32_e32 v199, v114
	v_mov_b32_e32 v200, v115
	v_mov_b32_e32 v201, v149
	v_mov_b32_e32 v202, v153
	v_mov_b32_e32 v203, v157
	v_mov_b32_e32 v204, v161
	v_mov_b32_e32 v205, v165
	v_mov_b32_e32 v206, v169
	v_mov_b32_e32 v207, v173
	v_mov_b32_e32 v208, v177
	v_mov_b32_e32 v209, v178
	v_mov_b32_e32 v210, v179
	v_mov_b32_e32 v211, v180
	v_mov_b32_e32 v212, v181
	v_mov_b32_e32 v214, v182
	v_mov_b32_e32 v215, v183
	v_mov_b32_e32 v216, v184
	v_mov_b32_e32 v218, v185
	v_readlane_b32 s76, v253, 4
	v_readlane_b32 s8, v253, 0
	v_readlane_b32 s9, v253, 1
	s_nop 1
	s_and_b32 s0, s76, 7
	s_lshr_b32 s1, s76, 3
	s_sub_i32 s1, s1, 24
	s_lshl_b32 s0, s0, 2
	s_lshr_b32 s2, s1, 1
	s_add_i32 s0, s0, s2
	s_and_b32 s1, s1, 1
	s_lshr_b32 s2, s0, 2
	s_lshl_b32 s2, s2, 3
	s_lshl_b32 s1, s1, 2
	s_and_b32 s0, s0, 3
	s_or_b32 s2, s2, s1
	s_or_b32 s76, s2, s0
	s_lshr_b32 s33, s78, 6
	s_movk_i32 s74, 64
	s_load_dwordx2 s[10:11], s[8:9], 0xa0
	v_mbcnt_lo_u32_b32 v69, -1, 0
	v_mbcnt_hi_u32_b32 v69, -1, v69
	s_mov_b64 exec, -1
	v_lshlrev_b32_e32 v76, 3, v69
	s_waitcnt lgkmcnt(0)
	s_branch .Lhp_common

; #define LAS __attribute__((address_space(3)))
; #define FRESH_TID() do { ap = fresh_args(); ws = ap->ws; unsigned m1_ = ~0u; asm volatile("" : "+s"(m1_)); lane = (int)__builtin_amdgcn_mbcnt_hi(m1_, __builtin_amdgcn_mbcnt_lo(m1_, 0u)); asm volatile("" : "+v"(lane)); wave = wave0; tid = wave0 * 64 + lane; } while (0)
; __device__ __forceinline__ void moe_table_build(LAS unsigned char* lds, const unsigned* cnt, int tid) {
;     ...
;     __syncthreads();
;     if (tid == 0) { int acc = 0; for (int e = 0; e < NE; ++e) { acc += (((LAS int*)(lds + MOE_TAB_OFF))[16 + e] + 255) >> 8; ((LAS int*)(lds + MOE_TAB_OFF))[e] = acc; } }
;     __syncthreads();
; }
;     __device__ __forceinline__ void init(LAS unsigned char* lds_, int nN_, int G_, int c_) {
;         lds = lds_; NT = __builtin_amdgcn_readfirstlane(((LAS int*)(lds + MOE_TAB_OFF))[15]); nN = nN_; G = G_; c = c_; }
; template <unsigned MASK, bool ONE>
; __global__ void __launch_bounds__(NTHREADS, 2) fwd_kernel(Args a_unused) {
;     ...
;         if (IN(P + 9, 10)) { FRESH_TID();
;             pg8::moe_table_build(lds, cntl, tid);
;             pg8::MoeOrder S; S.init(lds, 8, G, bx); pg8::RowsContig AM; pg8::EpiPlainS E{Y, pg8::W8_INV};
.LBB0_1010:
	s_or_b64 exec, exec, s[0:1]
	v_readlane_b32 s0, v254, 58
	s_waitcnt lgkmcnt(0)
	s_barrier
	v_mov_b32_e32 v2, s0
	ds_read_b32 v2, v2
	v_readlane_b32 s1, v253, 4
	v_readfirstlane_b32 s14, v1
	v_readlane_b32 s65, v255, 22
	s_movk_i32 s66, 0x179
	s_waitcnt lgkmcnt(0)
	v_readfirstlane_b32 s16, v2
	s_lshl_b32 s0, s16, 3
	s_cmp_eq_u32 s101, 0
	s_cbranch_scc1 .Lno_help10
	s_cmpk_lt_i32 s1, 0xc0
	s_cbranch_scc1 .Lno_help10
	s_movk_i32 s100, 0x4600
	s_movk_i32 s101, 0x6800
	s_mov_b32 s62, 0x20600000
	s_mov_b32 s0, 1
	v_writelane_b32 v251, s0, 30
	s_branch .Lhp_entry
